# baseline (speedup 1.0000x reference)
_Z8dog_mainPKfS0_S0_S0_S0_S0_S0_Pf:
	s_load_dwordx8 s[12:19], s[0:1], 0x0
	s_load_dwordx8 s[20:27], s[0:1], 0x20
	s_and_b32 s3, s2, 7
	s_lshl_b32 s3, s3, 5
	s_lshr_b32 s4, s2, 3
	s_add_i32 s4, s3, s4
	s_and_b32 s6, s4, 3
	s_lshr_b32 s7, s4, 2
	s_mov_b32 s5, 0
	s_lshl_b64 s[8:9], s[4:5], 18
	v_and_b32_e32 v1, 63, v0
	v_lshrrev_b32_e32 v2, 6, v0
	v_and_b32_e32 v3, 15, v0
	v_and_b32_e32 v7, 31, v0
	v_lshl_or_b32 v5, v2, 5, v7
	v_lshlrev_b32_e32 v5, 2, v5
	v_mov_b32_e32 v4, v5
	v_lshlrev_b32_e32 v6, 4, v1
	v_lshl_or_b32 v6, v2, 12, v6
	v_bfe_u32 v7, v0, 4, 2
	v_readfirstlane_b32 s28, v2
	s_cmp_ge_u32 s28, 4
	s_cbranch_scc0 .Lprio_skip
	s_setprio 1
.Lprio_skip:
	s_waitcnt lgkmcnt(0)
	global_load_dword v32, v4, s[18:19]
	global_load_dword v33, v4, s[20:21]
	global_load_dword v34, v4, s[22:23]
	global_load_dword v35, v4, s[24:25]
	global_load_dword v36, v4, s[14:15]
	global_load_dword v37, v4, s[16:17]
	s_add_u32 s12, s12, s8
	s_addc_u32 s13, s13, s9
	global_load_dwordx4 v[128:131], v6, s[12:13] offset:0 nt
	global_load_dwordx4 v[132:135], v6, s[12:13] offset:1024 nt
	global_load_dwordx4 v[136:139], v6, s[12:13] offset:2048 nt
	global_load_dwordx4 v[140:143], v6, s[12:13] offset:3072 nt
	v_add_u32_e32 v6, 0x8000, v6
	global_load_dwordx4 v[144:147], v6, s[12:13] offset:0 nt
	global_load_dwordx4 v[148:151], v6, s[12:13] offset:1024 nt
	global_load_dwordx4 v[152:155], v6, s[12:13] offset:2048 nt
	global_load_dwordx4 v[156:159], v6, s[12:13] offset:3072 nt
	v_and_b32_e32 v16, 1, v0
	v_cmp_eq_u32_e64 s[30:31], 0, v16
	v_and_b32_e32 v17, 2, v0
	v_cmp_eq_u32_e64 s[32:33], 0, v17
	v_and_b32_e32 v16, 3, v0
	v_lshrrev_b32_e32 v17, 2, v1
	v_lshlrev_b32_e32 v16, 5, v16
	v_lshl_add_u32 v16, v17, 1, v16
	v_lshrrev_b32_e32 v17, 1, v2
	s_movk_i32 s10, 0x110
	v_mad_u32_u24 v16, v17, s10, v16
	v_and_b32_e32 v17, 1, v2
	v_lshl_add_u32 v14, v17, 7, v16
	v_lshlrev_b32_e32 v17, 4, v7
	v_mad_u32_u24 v15, v3, s10, v17
	s_lshl_b32 s11, s6, 5
	v_lshl_add_u32 v18, v7, 2, s11
	v_cvt_f32_u32_e32 v18, v18
	v_lshlrev_b32_e32 v19, 3, v7
	v_cvt_f32_u32_e32 v19, v19
	s_waitcnt vmcnt(8)
	v_lshlrev_b32_e32 v16, 2, v3
	v_add_u32_e32 v17, 64, v16
	ds_bpermute_b32 v40, v16, v32
	ds_bpermute_b32 v46, v17, v32
	ds_bpermute_b32 v41, v16, v33
	ds_bpermute_b32 v47, v17, v33
	ds_bpermute_b32 v42, v16, v34
	ds_bpermute_b32 v48, v17, v34
	ds_bpermute_b32 v43, v16, v35
	ds_bpermute_b32 v49, v17, v35
	ds_bpermute_b32 v44, v16, v36
	ds_bpermute_b32 v50, v17, v36
	ds_bpermute_b32 v45, v16, v37
	ds_bpermute_b32 v51, v17, v37
	s_waitcnt lgkmcnt(0)
	v_add_f32_e32 v41, v40, v41
	v_sub_f32_e32 v12, v19, v42
	v_sub_f32_e32 v13, v18, v43
	v_rcp_f32_e32 v42, v40
	v_rcp_f32_e32 v43, v41
	s_nop 0
	v_fma_f32 v20, -v40, v42, 1.0
	v_fma_f32 v42, v20, v42, v42
	v_fma_f32 v20, -v41, v43, 1.0
	v_fma_f32 v43, v20, v43, v43
	v_mul_f32_e32 v8, 0xbf38aa3b, v42
	v_mul_f32_e32 v9, 0xbf38aa3b, v43
	v_mul_f32_e32 v44, v44, v42
	v_mul_f32_e32 v45, v45, v43
	v_mul_f32_e32 v10, 0x3e22f983, v44
	v_mul_f32_e32 v11, 0x3e22f983, v45
	v_add_f32_e32 v47, v46, v47
	v_sub_f32_e32 v2, v19, v48
	v_sub_f32_e32 v3, v18, v49
	v_rcp_f32_e32 v48, v46
	v_rcp_f32_e32 v49, v47
	s_nop 0
	v_fma_f32 v20, -v46, v48, 1.0
	v_fma_f32 v48, v20, v48, v48
	v_fma_f32 v20, -v47, v49, 1.0
	v_fma_f32 v49, v20, v49, v49
	v_mul_f32_e32 v28, 0xbf38aa3b, v48
	v_mul_f32_e32 v29, 0xbf38aa3b, v49
	v_mul_f32_e32 v50, v50, v48
	v_mul_f32_e32 v51, v51, v49
	v_mul_f32_e32 v30, 0x3e22f983, v50
	v_mul_f32_e32 v31, 0x3e22f983, v51
	s_getpc_b64 s[44:45]
